# attention q-block epilogue rewritten: per-lane fp8 packing of four rows then quad byte transpose (DPP + v_perm), 16 full-wave dword stores instead of 64 quarter-masked ones; on top of v32
# baseline (speedup 1.0000x reference)
.LBB0_817:
	s_or_b64 exec, exec, s[56:57]
	s_waitcnt lgkmcnt(0)
	s_lshl_b64 s[0:1], s[54:55], 11
	s_add_u32 s0, s61, s0
	s_addc_u32 s1, s62, s1
	s_add_u32 s0, s0, s79
	s_addc_u32 s1, s1, 0
	s_mov_b32 s56, 0x05040100
	v_and_b32_e32 v85, 3, v164
	v_lshl_add_u32 v83, v85, 8, v85
	v_add_u32_e32 v83, 0x0c0c0400, v83
	v_lshrrev_b32_e32 v87, 5, v164
	v_lshl_add_u32 v84, v87, 2, v85
	v_lshlrev_b32_e32 v84, 11, v84
	v_and_b32_e32 v85, 28, v164
	v_add_u32_e32 v84, v84, v85
	v_lshl_add_u32 v87, v87, 4, s65
	ds_read_b128 v[66:69], v87 offset:128
	v_mov_b32_e32 v86, v84
	s_waitcnt lgkmcnt(0)
	v_mul_f32_e32 v66, 0x41800000, v66
	v_mul_f32_e32 v67, 0x41800000, v67
	v_mul_f32_e32 v68, 0x41800000, v68
	v_mul_f32_e32 v69, 0x41800000, v69
	v_mul_f32_e32 v70, v50, v66
	v_mul_f32_e32 v71, v51, v67
	v_mul_f32_e32 v72, v52, v68
	v_mul_f32_e32 v73, v53, v69
	v_med3_f32 v70, v70, s77, v166
	v_med3_f32 v71, v71, s77, v166
	v_med3_f32 v72, v72, s77, v166
	v_med3_f32 v73, v73, s77, v166
	v_cvt_pk_fp8_f32 v74, v70, v71
	v_cvt_pk_fp8_f32 v74, v72, v73 op_sel:[0,0,1]
	s_nop 1
	v_mov_b32_dpp v75, v74 quad_perm:[0,0,0,0] row_mask:0xf bank_mask:0xf
	v_mov_b32_dpp v76, v74 quad_perm:[1,1,1,1] row_mask:0xf bank_mask:0xf
	v_mov_b32_dpp v77, v74 quad_perm:[2,2,2,2] row_mask:0xf bank_mask:0xf
	v_mov_b32_dpp v78, v74 quad_perm:[3,3,3,3] row_mask:0xf bank_mask:0xf
	v_perm_b32 v80, v76, v75, v83
	v_perm_b32 v81, v78, v77, v83
	v_perm_b32 v82, v81, v80, s56
	global_store_dword v86, v82, s[0:1]
	v_mul_f32_e32 v70, v34, v66
	v_mul_f32_e32 v71, v35, v67
	v_mul_f32_e32 v72, v36, v68
	v_mul_f32_e32 v73, v37, v69
	v_med3_f32 v70, v70, s77, v166
	v_med3_f32 v71, v71, s77, v166
	v_med3_f32 v72, v72, s77, v166
	v_med3_f32 v73, v73, s77, v166
	v_cvt_pk_fp8_f32 v74, v70, v71
	v_cvt_pk_fp8_f32 v74, v72, v73 op_sel:[0,0,1]
	s_nop 1
	v_mov_b32_dpp v75, v74 quad_perm:[0,0,0,0] row_mask:0xf bank_mask:0xf
	v_mov_b32_dpp v76, v74 quad_perm:[1,1,1,1] row_mask:0xf bank_mask:0xf
	v_mov_b32_dpp v77, v74 quad_perm:[2,2,2,2] row_mask:0xf bank_mask:0xf
	v_mov_b32_dpp v78, v74 quad_perm:[3,3,3,3] row_mask:0xf bank_mask:0xf
	v_perm_b32 v80, v76, v75, v83
	v_perm_b32 v81, v78, v77, v83
	v_perm_b32 v82, v81, v80, s56
	global_store_dword v86, v82, s[0:1] offset:32
	v_mul_f32_e32 v70, v18, v66
	v_mul_f32_e32 v71, v19, v67
	v_mul_f32_e32 v72, v20, v68
	v_mul_f32_e32 v73, v21, v69
	v_med3_f32 v70, v70, s77, v166
	v_med3_f32 v71, v71, s77, v166
	v_med3_f32 v72, v72, s77, v166
	v_med3_f32 v73, v73, s77, v166
	v_cvt_pk_fp8_f32 v74, v70, v71
	v_cvt_pk_fp8_f32 v74, v72, v73 op_sel:[0,0,1]
	s_nop 1
	v_mov_b32_dpp v75, v74 quad_perm:[0,0,0,0] row_mask:0xf bank_mask:0xf
	v_mov_b32_dpp v76, v74 quad_perm:[1,1,1,1] row_mask:0xf bank_mask:0xf
	v_mov_b32_dpp v77, v74 quad_perm:[2,2,2,2] row_mask:0xf bank_mask:0xf
	v_mov_b32_dpp v78, v74 quad_perm:[3,3,3,3] row_mask:0xf bank_mask:0xf
	v_perm_b32 v80, v76, v75, v83
	v_perm_b32 v81, v78, v77, v83
	v_perm_b32 v82, v81, v80, s56
	global_store_dword v86, v82, s[0:1] offset:64
	v_mul_f32_e32 v70, v2, v66
	v_mul_f32_e32 v71, v3, v67
	v_mul_f32_e32 v72, v4, v68
	v_mul_f32_e32 v73, v5, v69
	v_med3_f32 v70, v70, s77, v166
	v_med3_f32 v71, v71, s77, v166
	v_med3_f32 v72, v72, s77, v166
	v_med3_f32 v73, v73, s77, v166
	v_cvt_pk_fp8_f32 v74, v70, v71
	v_cvt_pk_fp8_f32 v74, v72, v73 op_sel:[0,0,1]
	s_nop 1
	v_mov_b32_dpp v75, v74 quad_perm:[0,0,0,0] row_mask:0xf bank_mask:0xf
	v_mov_b32_dpp v76, v74 quad_perm:[1,1,1,1] row_mask:0xf bank_mask:0xf
	v_mov_b32_dpp v77, v74 quad_perm:[2,2,2,2] row_mask:0xf bank_mask:0xf
	v_mov_b32_dpp v78, v74 quad_perm:[3,3,3,3] row_mask:0xf bank_mask:0xf
	v_perm_b32 v80, v76, v75, v83
	v_perm_b32 v81, v78, v77, v83
	v_perm_b32 v82, v81, v80, s56
	global_store_dword v86, v82, s[0:1] offset:96
	ds_read_b128 v[66:69], v87 offset:160
	v_add_u32_e32 v86, 0x4000, v84
	s_waitcnt lgkmcnt(0)
	v_mul_f32_e32 v66, 0x41800000, v66
	v_mul_f32_e32 v67, 0x41800000, v67
	v_mul_f32_e32 v68, 0x41800000, v68
	v_mul_f32_e32 v69, 0x41800000, v69
	v_mul_f32_e32 v70, v54, v66
	v_mul_f32_e32 v71, v55, v67
	v_mul_f32_e32 v72, v56, v68
	v_mul_f32_e32 v73, v57, v69
	v_med3_f32 v70, v70, s77, v166
	v_med3_f32 v71, v71, s77, v166
	v_med3_f32 v72, v72, s77, v166
	v_med3_f32 v73, v73, s77, v166
	v_cvt_pk_fp8_f32 v74, v70, v71
	v_cvt_pk_fp8_f32 v74, v72, v73 op_sel:[0,0,1]
	s_nop 1
	v_mov_b32_dpp v75, v74 quad_perm:[0,0,0,0] row_mask:0xf bank_mask:0xf
	v_mov_b32_dpp v76, v74 quad_perm:[1,1,1,1] row_mask:0xf bank_mask:0xf
	v_mov_b32_dpp v77, v74 quad_perm:[2,2,2,2] row_mask:0xf bank_mask:0xf
	v_mov_b32_dpp v78, v74 quad_perm:[3,3,3,3] row_mask:0xf bank_mask:0xf
	v_perm_b32 v80, v76, v75, v83
	v_perm_b32 v81, v78, v77, v83
	v_perm_b32 v82, v81, v80, s56
	global_store_dword v86, v82, s[0:1]
	v_mul_f32_e32 v70, v38, v66
	v_mul_f32_e32 v71, v39, v67
	v_mul_f32_e32 v72, v40, v68
	v_mul_f32_e32 v73, v41, v69
	v_med3_f32 v70, v70, s77, v166
	v_med3_f32 v71, v71, s77, v166
	v_med3_f32 v72, v72, s77, v166
	v_med3_f32 v73, v73, s77, v166
	v_cvt_pk_fp8_f32 v74, v70, v71
	v_cvt_pk_fp8_f32 v74, v72, v73 op_sel:[0,0,1]
	s_nop 1
	v_mov_b32_dpp v75, v74 quad_perm:[0,0,0,0] row_mask:0xf bank_mask:0xf
	v_mov_b32_dpp v76, v74 quad_perm:[1,1,1,1] row_mask:0xf bank_mask:0xf
	v_mov_b32_dpp v77, v74 quad_perm:[2,2,2,2] row_mask:0xf bank_mask:0xf
	v_mov_b32_dpp v78, v74 quad_perm:[3,3,3,3] row_mask:0xf bank_mask:0xf
	v_perm_b32 v80, v76, v75, v83
	v_perm_b32 v81, v78, v77, v83
	v_perm_b32 v82, v81, v80, s56
	global_store_dword v86, v82, s[0:1] offset:32
	v_mul_f32_e32 v70, v22, v66
	v_mul_f32_e32 v71, v23, v67
	v_mul_f32_e32 v72, v24, v68
	v_mul_f32_e32 v73, v25, v69
	v_med3_f32 v70, v70, s77, v166
	v_med3_f32 v71, v71, s77, v166
	v_med3_f32 v72, v72, s77, v166
	v_med3_f32 v73, v73, s77, v166
	v_cvt_pk_fp8_f32 v74, v70, v71
	v_cvt_pk_fp8_f32 v74, v72, v73 op_sel:[0,0,1]
	s_nop 1
	v_mov_b32_dpp v75, v74 quad_perm:[0,0,0,0] row_mask:0xf bank_mask:0xf
	v_mov_b32_dpp v76, v74 quad_perm:[1,1,1,1] row_mask:0xf bank_mask:0xf
	v_mov_b32_dpp v77, v74 quad_perm:[2,2,2,2] row_mask:0xf bank_mask:0xf
	v_mov_b32_dpp v78, v74 quad_perm:[3,3,3,3] row_mask:0xf bank_mask:0xf
	v_perm_b32 v80, v76, v75, v83
	v_perm_b32 v81, v78, v77, v83
	v_perm_b32 v82, v81, v80, s56
	global_store_dword v86, v82, s[0:1] offset:64
	v_mul_f32_e32 v70, v6, v66
	v_mul_f32_e32 v71, v7, v67
	v_mul_f32_e32 v72, v8, v68
	v_mul_f32_e32 v73, v9, v69
	v_med3_f32 v70, v70, s77, v166
	v_med3_f32 v71, v71, s77, v166
	v_med3_f32 v72, v72, s77, v166
	v_med3_f32 v73, v73, s77, v166
	v_cvt_pk_fp8_f32 v74, v70, v71
	v_cvt_pk_fp8_f32 v74, v72, v73 op_sel:[0,0,1]
	s_nop 1
	v_mov_b32_dpp v75, v74 quad_perm:[0,0,0,0] row_mask:0xf bank_mask:0xf
	v_mov_b32_dpp v76, v74 quad_perm:[1,1,1,1] row_mask:0xf bank_mask:0xf
	v_mov_b32_dpp v77, v74 quad_perm:[2,2,2,2] row_mask:0xf bank_mask:0xf
	v_mov_b32_dpp v78, v74 quad_perm:[3,3,3,3] row_mask:0xf bank_mask:0xf
	v_perm_b32 v80, v76, v75, v83
	v_perm_b32 v81, v78, v77, v83
	v_perm_b32 v82, v81, v80, s56
	global_store_dword v86, v82, s[0:1] offset:96
	ds_read_b128 v[66:69], v87 offset:192
	v_add_u32_e32 v86, 0x8000, v84
	s_waitcnt lgkmcnt(0)
	v_mul_f32_e32 v66, 0x41800000, v66
	v_mul_f32_e32 v67, 0x41800000, v67
	v_mul_f32_e32 v68, 0x41800000, v68
	v_mul_f32_e32 v69, 0x41800000, v69
	v_mul_f32_e32 v70, v58, v66
	v_mul_f32_e32 v71, v59, v67
	v_mul_f32_e32 v72, v60, v68
	v_mul_f32_e32 v73, v61, v69
	v_med3_f32 v70, v70, s77, v166
	v_med3_f32 v71, v71, s77, v166
	v_med3_f32 v72, v72, s77, v166
	v_med3_f32 v73, v73, s77, v166
	v_cvt_pk_fp8_f32 v74, v70, v71
	v_cvt_pk_fp8_f32 v74, v72, v73 op_sel:[0,0,1]
	s_nop 1
	v_mov_b32_dpp v75, v74 quad_perm:[0,0,0,0] row_mask:0xf bank_mask:0xf
	v_mov_b32_dpp v76, v74 quad_perm:[1,1,1,1] row_mask:0xf bank_mask:0xf
	v_mov_b32_dpp v77, v74 quad_perm:[2,2,2,2] row_mask:0xf bank_mask:0xf
	v_mov_b32_dpp v78, v74 quad_perm:[3,3,3,3] row_mask:0xf bank_mask:0xf
	v_perm_b32 v80, v76, v75, v83
	v_perm_b32 v81, v78, v77, v83
	v_perm_b32 v82, v81, v80, s56
	global_store_dword v86, v82, s[0:1]
	v_mul_f32_e32 v70, v42, v66
	v_mul_f32_e32 v71, v43, v67
	v_mul_f32_e32 v72, v44, v68
	v_mul_f32_e32 v73, v45, v69
	v_med3_f32 v70, v70, s77, v166
	v_med3_f32 v71, v71, s77, v166
	v_med3_f32 v72, v72, s77, v166
	v_med3_f32 v73, v73, s77, v166
	v_cvt_pk_fp8_f32 v74, v70, v71
	v_cvt_pk_fp8_f32 v74, v72, v73 op_sel:[0,0,1]
	s_nop 1
	v_mov_b32_dpp v75, v74 quad_perm:[0,0,0,0] row_mask:0xf bank_mask:0xf
	v_mov_b32_dpp v76, v74 quad_perm:[1,1,1,1] row_mask:0xf bank_mask:0xf
	v_mov_b32_dpp v77, v74 quad_perm:[2,2,2,2] row_mask:0xf bank_mask:0xf
	v_mov_b32_dpp v78, v74 quad_perm:[3,3,3,3] row_mask:0xf bank_mask:0xf
	v_perm_b32 v80, v76, v75, v83
	v_perm_b32 v81, v78, v77, v83
	v_perm_b32 v82, v81, v80, s56
	global_store_dword v86, v82, s[0:1] offset:32
	v_mul_f32_e32 v70, v26, v66
	v_mul_f32_e32 v71, v27, v67
	v_mul_f32_e32 v72, v28, v68
	v_mul_f32_e32 v73, v29, v69
	v_med3_f32 v70, v70, s77, v166
	v_med3_f32 v71, v71, s77, v166
	v_med3_f32 v72, v72, s77, v166
	v_med3_f32 v73, v73, s77, v166
	v_cvt_pk_fp8_f32 v74, v70, v71
	v_cvt_pk_fp8_f32 v74, v72, v73 op_sel:[0,0,1]
	s_nop 1
	v_mov_b32_dpp v75, v74 quad_perm:[0,0,0,0] row_mask:0xf bank_mask:0xf
	v_mov_b32_dpp v76, v74 quad_perm:[1,1,1,1] row_mask:0xf bank_mask:0xf
	v_mov_b32_dpp v77, v74 quad_perm:[2,2,2,2] row_mask:0xf bank_mask:0xf
	v_mov_b32_dpp v78, v74 quad_perm:[3,3,3,3] row_mask:0xf bank_mask:0xf
	v_perm_b32 v80, v76, v75, v83
	v_perm_b32 v81, v78, v77, v83
	v_perm_b32 v82, v81, v80, s56
	global_store_dword v86, v82, s[0:1] offset:64
	v_mul_f32_e32 v70, v10, v66
	v_mul_f32_e32 v71, v11, v67
	v_mul_f32_e32 v72, v12, v68
	v_mul_f32_e32 v73, v13, v69
	v_med3_f32 v70, v70, s77, v166
	v_med3_f32 v71, v71, s77, v166
	v_med3_f32 v72, v72, s77, v166
	v_med3_f32 v73, v73, s77, v166
	v_cvt_pk_fp8_f32 v74, v70, v71
	v_cvt_pk_fp8_f32 v74, v72, v73 op_sel:[0,0,1]
	s_nop 1
	v_mov_b32_dpp v75, v74 quad_perm:[0,0,0,0] row_mask:0xf bank_mask:0xf
	v_mov_b32_dpp v76, v74 quad_perm:[1,1,1,1] row_mask:0xf bank_mask:0xf
	v_mov_b32_dpp v77, v74 quad_perm:[2,2,2,2] row_mask:0xf bank_mask:0xf
	v_mov_b32_dpp v78, v74 quad_perm:[3,3,3,3] row_mask:0xf bank_mask:0xf
	v_perm_b32 v80, v76, v75, v83
	v_perm_b32 v81, v78, v77, v83
	v_perm_b32 v82, v81, v80, s56
	global_store_dword v86, v82, s[0:1] offset:96
	ds_read_b128 v[66:69], v87 offset:224
	v_add_u32_e32 v86, 0xc000, v84
	s_waitcnt lgkmcnt(0)
	v_mul_f32_e32 v66, 0x41800000, v66
	v_mul_f32_e32 v67, 0x41800000, v67
	v_mul_f32_e32 v68, 0x41800000, v68
	v_mul_f32_e32 v69, 0x41800000, v69
	v_mul_f32_e32 v70, v62, v66
	v_mul_f32_e32 v71, v63, v67
	v_mul_f32_e32 v72, v64, v68
	v_mul_f32_e32 v73, v65, v69
	v_med3_f32 v70, v70, s77, v166
	v_med3_f32 v71, v71, s77, v166
	v_med3_f32 v72, v72, s77, v166
	v_med3_f32 v73, v73, s77, v166
	v_cvt_pk_fp8_f32 v74, v70, v71
	v_cvt_pk_fp8_f32 v74, v72, v73 op_sel:[0,0,1]
	s_nop 1
	v_mov_b32_dpp v75, v74 quad_perm:[0,0,0,0] row_mask:0xf bank_mask:0xf
	v_mov_b32_dpp v76, v74 quad_perm:[1,1,1,1] row_mask:0xf bank_mask:0xf
	v_mov_b32_dpp v77, v74 quad_perm:[2,2,2,2] row_mask:0xf bank_mask:0xf
	v_mov_b32_dpp v78, v74 quad_perm:[3,3,3,3] row_mask:0xf bank_mask:0xf
	v_perm_b32 v80, v76, v75, v83
	v_perm_b32 v81, v78, v77, v83
	v_perm_b32 v82, v81, v80, s56
	global_store_dword v86, v82, s[0:1]
	v_mul_f32_e32 v70, v46, v66
	v_mul_f32_e32 v71, v47, v67
	v_mul_f32_e32 v72, v48, v68
	v_mul_f32_e32 v73, v49, v69
	v_med3_f32 v70, v70, s77, v166
	v_med3_f32 v71, v71, s77, v166
	v_med3_f32 v72, v72, s77, v166
	v_med3_f32 v73, v73, s77, v166
	v_cvt_pk_fp8_f32 v74, v70, v71
	v_cvt_pk_fp8_f32 v74, v72, v73 op_sel:[0,0,1]
	s_nop 1
	v_mov_b32_dpp v75, v74 quad_perm:[0,0,0,0] row_mask:0xf bank_mask:0xf
	v_mov_b32_dpp v76, v74 quad_perm:[1,1,1,1] row_mask:0xf bank_mask:0xf
	v_mov_b32_dpp v77, v74 quad_perm:[2,2,2,2] row_mask:0xf bank_mask:0xf
	v_mov_b32_dpp v78, v74 quad_perm:[3,3,3,3] row_mask:0xf bank_mask:0xf
	v_perm_b32 v80, v76, v75, v83
	v_perm_b32 v81, v78, v77, v83
	v_perm_b32 v82, v81, v80, s56
	global_store_dword v86, v82, s[0:1] offset:32
	v_mul_f32_e32 v70, v30, v66
	v_mul_f32_e32 v71, v31, v67
	v_mul_f32_e32 v72, v32, v68
	v_mul_f32_e32 v73, v33, v69
	v_med3_f32 v70, v70, s77, v166
	v_med3_f32 v71, v71, s77, v166
	v_med3_f32 v72, v72, s77, v166
	v_med3_f32 v73, v73, s77, v166
	v_cvt_pk_fp8_f32 v74, v70, v71
	v_cvt_pk_fp8_f32 v74, v72, v73 op_sel:[0,0,1]
	s_nop 1
	v_mov_b32_dpp v75, v74 quad_perm:[0,0,0,0] row_mask:0xf bank_mask:0xf
	v_mov_b32_dpp v76, v74 quad_perm:[1,1,1,1] row_mask:0xf bank_mask:0xf
	v_mov_b32_dpp v77, v74 quad_perm:[2,2,2,2] row_mask:0xf bank_mask:0xf
	v_mov_b32_dpp v78, v74 quad_perm:[3,3,3,3] row_mask:0xf bank_mask:0xf
	v_perm_b32 v80, v76, v75, v83
	v_perm_b32 v81, v78, v77, v83
	v_perm_b32 v82, v81, v80, s56
	global_store_dword v86, v82, s[0:1] offset:64
	v_mul_f32_e32 v70, v14, v66
	v_mul_f32_e32 v71, v15, v67
	v_mul_f32_e32 v72, v16, v68
	v_mul_f32_e32 v73, v17, v69
	v_med3_f32 v70, v70, s77, v166
	v_med3_f32 v71, v71, s77, v166
	v_med3_f32 v72, v72, s77, v166
	v_med3_f32 v73, v73, s77, v166
	v_cvt_pk_fp8_f32 v74, v70, v71
	v_cvt_pk_fp8_f32 v74, v72, v73 op_sel:[0,0,1]
	s_nop 1
	v_mov_b32_dpp v75, v74 quad_perm:[0,0,0,0] row_mask:0xf bank_mask:0xf
	v_mov_b32_dpp v76, v74 quad_perm:[1,1,1,1] row_mask:0xf bank_mask:0xf
	v_mov_b32_dpp v77, v74 quad_perm:[2,2,2,2] row_mask:0xf bank_mask:0xf
	v_mov_b32_dpp v78, v74 quad_perm:[3,3,3,3] row_mask:0xf bank_mask:0xf
	v_perm_b32 v80, v76, v75, v83
	v_perm_b32 v81, v78, v77, v83
	v_perm_b32 v82, v81, v80, s56
	global_store_dword v86, v82, s[0:1] offset:96


	s_lshl_b32 s55, s80, 8
	s_and_b32 s0, s81, 15
	s_add_i32 s55, s55, s63
	s_lshl_b32 s54, s0, 8
	v_mov_b32_e32 v168, v1
	s_ashr_i32 s0, s55, 31
	s_add_u32 s52, s52, s55
	v_and_b32_e32 v167, 31, v168
	v_or_b32_e32 v30, s52, v167
	v_mov_b64_e32 v[2:3], s[6:7]
	s_addc_u32 s53, s53, s0
	v_mad_u64_u32 v[2:3], s[0:1], v30, s68, v[2:3]
	v_bfe_u32 v169, v168, 5, 1
	v_mad_i32_i24 v3, s53, v162, v3
	s_lshl_b32 s12, s82, 1
	v_lshl_add_u64 v[2:3], v[2:3], 0, s[12:13]
	v_lshlrev_b32_e32 v148, 4, v169
	v_lshl_add_u64 v[44:45], v[2:3], 0, v[148:149]
	global_load_dwordx4 v[32:35], v[44:45], off
	global_load_dwordx4 v[36:39], v[44:45], off offset:32
	global_load_dwordx4 v[26:29], v[44:45], off offset:64
	global_load_dwordx4 v[22:25], v[44:45], off offset:96
	global_load_dwordx4 v[18:21], v[44:45], off offset:128
	global_load_dwordx4 v[14:17], v[44:45], off offset:160
	global_load_dwordx4 v[10:13], v[44:45], off offset:192
	v_and_b32_e32 v118, 32, v168
	global_load_dwordx4 v[6:9], v118, s[4:5] offset:576
	s_waitcnt lgkmcnt(0)
	global_load_dwordx4 v[2:5], v118, s[4:5] offset:592
	global_load_dwordx4 v[102:105], v118, s[4:5] offset:704
	global_load_dwordx4 v[110:113], v118, s[4:5] offset:720
	global_load_dwordx4 v[40:43], v[44:45], off offset:224
	global_load_dwordx4 v[82:85], v[44:45], off offset:256
	global_load_dwordx4 v[138:141], v[44:45], off offset:288
	global_load_dwordx4 v[70:73], v[44:45], off offset:320
	global_load_dwordx4 v[142:145], v[44:45], off offset:352
	v_mov_b32_e32 v31, s53
	s_mov_b32 m0, s71
	s_mov_b32 s12, 1
	s_waitcnt vmcnt(0)
	v_and_b32_e32 v191, 0xffff0000, v32
	v_lshlrev_b32_e32 v190, 16, v32
	v_lshlrev_b32_e32 v206, 16, v26
	v_and_b32_e32 v207, 0xffff0000, v26
	v_lshlrev_b32_e32 v208, 16, v27
	v_and_b32_e32 v209, 0xffff0000, v27
	v_lshlrev_b32_e32 v210, 16, v28
	v_and_b32_e32 v211, 0xffff0000, v28
	v_lshlrev_b32_e32 v212, 16, v29
	v_and_b32_e32 v213, 0xffff0000, v29
	v_lshlrev_b32_e32 v222, 16, v18
	v_and_b32_e32 v223, 0xffff0000, v18
	v_lshlrev_b32_e32 v224, 16, v19
	v_and_b32_e32 v225, 0xffff0000, v19
	v_lshlrev_b32_e32 v226, 16, v20
	v_and_b32_e32 v227, 0xffff0000, v20
	v_lshlrev_b32_e32 v228, 16, v21
	v_and_b32_e32 v229, 0xffff0000, v21
	global_load_dwordx4 v[26:29], v118, s[4:5] offset:640
	global_load_dwordx4 v[156:159], v118, s[4:5] offset:656
	global_load_dwordx4 v[18:21], v118, s[4:5] offset:528
	v_mul_f32_e32 v188, v191, v191
	v_lshlrev_b32_e32 v192, 16, v33
	v_fmac_f32_e32 v188, v190, v190
	v_and_b32_e32 v193, 0xffff0000, v33
	v_fmac_f32_e32 v188, v192, v192
	v_lshlrev_b32_e32 v194, 16, v34
	v_fmac_f32_e32 v188, v193, v193
	v_and_b32_e32 v195, 0xffff0000, v34
	v_fmac_f32_e32 v188, v194, v194
	v_lshlrev_b32_e32 v196, 16, v35
	v_fmac_f32_e32 v188, v195, v195
	v_and_b32_e32 v197, 0xffff0000, v35
	v_fmac_f32_e32 v188, v196, v196
	v_lshlrev_b32_e32 v198, 16, v36
	v_fmac_f32_e32 v188, v197, v197
	v_and_b32_e32 v199, 0xffff0000, v36
	v_fmac_f32_e32 v188, v198, v198
	v_lshlrev_b32_e32 v200, 16, v37
	v_lshlrev_b32_e32 v214, 16, v22
	v_and_b32_e32 v215, 0xffff0000, v22
	v_lshlrev_b32_e32 v216, 16, v23
	v_and_b32_e32 v217, 0xffff0000, v23
	v_lshlrev_b32_e32 v218, 16, v24
	v_and_b32_e32 v219, 0xffff0000, v24
	v_lshlrev_b32_e32 v220, 16, v25
	v_and_b32_e32 v221, 0xffff0000, v25
	v_fmac_f32_e32 v188, v199, v199
	global_load_dwordx4 v[22:25], v118, s[4:5] offset:512
	v_and_b32_e32 v201, 0xffff0000, v37
	v_fmac_f32_e32 v188, v200, v200
	v_lshlrev_b32_e32 v202, 16, v38
	v_fmac_f32_e32 v188, v201, v201
	v_and_b32_e32 v203, 0xffff0000, v38
	v_fmac_f32_e32 v188, v202, v202
	v_lshlrev_b32_e32 v204, 16, v39
	v_fmac_f32_e32 v188, v203, v203
	v_and_b32_e32 v205, 0xffff0000, v39
	v_fmac_f32_e32 v188, v204, v204
	v_fmac_f32_e32 v188, v205, v205
	v_fmac_f32_e32 v188, v206, v206
	v_fmac_f32_e32 v188, v207, v207
	v_fmac_f32_e32 v188, v208, v208
	v_fmac_f32_e32 v188, v209, v209
	v_fmac_f32_e32 v188, v210, v210
	v_fmac_f32_e32 v188, v211, v211
	v_fmac_f32_e32 v188, v212, v212
	v_fmac_f32_e32 v188, v213, v213
	v_fmac_f32_e32 v188, v214, v214
	v_fmac_f32_e32 v188, v215, v215
	v_fmac_f32_e32 v188, v216, v216
	v_fmac_f32_e32 v188, v217, v217
	v_fmac_f32_e32 v188, v218, v218
	v_fmac_f32_e32 v188, v219, v219
	v_fmac_f32_e32 v188, v220, v220
	v_fmac_f32_e32 v188, v221, v221
	v_fmac_f32_e32 v188, v222, v222
	v_fmac_f32_e32 v188, v223, v223
	v_fmac_f32_e32 v188, v224, v224
	v_fmac_f32_e32 v188, v225, v225
	v_fmac_f32_e32 v188, v226, v226
	v_fmac_f32_e32 v188, v227, v227
	v_fmac_f32_e32 v188, v228, v228
	v_lshlrev_b32_e32 v230, 16, v14
	v_fmac_f32_e32 v188, v229, v229
	v_and_b32_e32 v231, 0xffff0000, v14
	v_fmac_f32_e32 v188, v230, v230
	v_lshlrev_b32_e32 v232, 16, v15
	v_fmac_f32_e32 v188, v231, v231
	v_and_b32_e32 v233, 0xffff0000, v15
	v_fmac_f32_e32 v188, v232, v232
	v_lshlrev_b32_e32 v234, 16, v16
	v_fmac_f32_e32 v188, v233, v233
	v_and_b32_e32 v235, 0xffff0000, v16
	v_fmac_f32_e32 v188, v234, v234
	v_lshlrev_b32_e32 v246, 16, v40
	v_and_b32_e32 v247, 0xffff0000, v40
	v_lshlrev_b32_e32 v248, 16, v41
	v_and_b32_e32 v249, 0xffff0000, v41
	v_lshlrev_b32_e32 v250, 16, v42
	v_and_b32_e32 v251, 0xffff0000, v42
	v_lshlrev_b32_e32 v252, 16, v43
	v_and_b32_e32 v253, 0xffff0000, v43
	global_load_dwordx4 v[106:109], v118, s[4:5] offset:16
	global_load_dwordx4 v[114:117], v118, s[4:5]
	global_load_dwordx4 v[94:97], v118, s[4:5] offset:80
	global_load_dwordx4 v[98:101], v118, s[4:5] offset:64
	global_load_dwordx4 v[86:89], v118, s[4:5] offset:144
	global_load_dwordx4 v[90:93], v118, s[4:5] offset:128
	global_load_dwordx4 v[74:77], v118, s[4:5] offset:208
	global_load_dwordx4 v[78:81], v118, s[4:5] offset:192
	global_load_dwordx4 v[62:65], v118, s[4:5] offset:272
	global_load_dwordx4 v[66:69], v118, s[4:5] offset:256
	global_load_dwordx4 v[54:57], v118, s[4:5] offset:336
	global_load_dwordx4 v[58:61], v118, s[4:5] offset:320
	global_load_dwordx4 v[46:49], v118, s[4:5] offset:400
	global_load_dwordx4 v[50:53], v118, s[4:5] offset:384
	global_load_dwordx4 v[38:41], v118, s[4:5] offset:464
	global_load_dwordx4 v[42:45], v118, s[4:5] offset:448
	v_lshlrev_b32_e32 v236, 16, v17
	v_fmac_f32_e32 v188, v235, v235
	v_and_b32_e32 v237, 0xffff0000, v17
	v_fmac_f32_e32 v188, v236, v236
	v_lshlrev_b32_e32 v238, 16, v10
	v_fmac_f32_e32 v188, v237, v237
	v_and_b32_e32 v239, 0xffff0000, v10
	v_fmac_f32_e32 v188, v238, v238
	v_lshlrev_b32_e32 v240, 16, v11
	v_fmac_f32_e32 v188, v239, v239
	v_and_b32_e32 v241, 0xffff0000, v11
	v_fmac_f32_e32 v188, v240, v240
	v_lshlrev_b32_e32 v242, 16, v12
	v_fmac_f32_e32 v188, v241, v241
	v_and_b32_e32 v243, 0xffff0000, v12
	v_fmac_f32_e32 v188, v242, v242
	v_lshlrev_b32_e32 v244, 16, v13
	v_fmac_f32_e32 v188, v243, v243
	v_and_b32_e32 v245, 0xffff0000, v13
	v_fmac_f32_e32 v188, v244, v244
	v_fmac_f32_e32 v188, v245, v245
	v_fmac_f32_e32 v188, v246, v246
	v_fmac_f32_e32 v188, v247, v247
	v_fmac_f32_e32 v188, v248, v248
	v_fmac_f32_e32 v188, v249, v249
	v_fmac_f32_e32 v188, v250, v250
	v_fmac_f32_e32 v188, v251, v251
	v_fmac_f32_e32 v188, v252, v252
	v_lshlrev_b32_e32 v187, 16, v82
	v_lshlrev_b32_e32 v186, 16, v70
	v_fmac_f32_e32 v188, v253, v253
	v_lshlrev_b32_e32 v124, 16, v144
	v_and_b32_e32 v126, 0xffff0000, v144
	v_lshlrev_b32_e32 v131, 16, v139
	v_and_b32_e32 v133, 0xffff0000, v139
	v_lshlrev_b32_e32 v137, 16, v138
	v_lshlrev_b32_e32 v136, 16, v142
	v_and_b32_e32 v139, 0xffff0000, v138
	v_and_b32_e32 v138, 0xffff0000, v142
	v_lshlrev_b32_e32 v142, 16, v73
	v_and_b32_e32 v144, 0xffff0000, v73
	v_lshlrev_b32_e32 v152, 16, v72
	v_and_b32_e32 v154, 0xffff0000, v72
	v_pk_mul_f32 v[72:73], v[186:187], v[186:187]
	s_waitcnt vmcnt(18)
	v_mov_b32_e32 v150, v158
	v_mov_b32_e32 v158, v156
	v_lshlrev_b32_e32 v156, 16, v71
	v_and_b32_e32 v184, 0xffff0000, v71
	v_and_b32_e32 v189, 0xffff0000, v82
	v_add_f32_e32 v71, v73, v188
	v_and_b32_e32 v188, 0xffff0000, v70
	v_mov_b32_e32 v128, v110
	v_mov_b32_e32 v129, v2
	v_mov_b32_e32 v2, v111
	s_waitcnt vmcnt(17)
	v_mov_b32_e32 v151, v20
	v_mov_b32_e32 v20, v159
	v_mov_b32_e32 v159, v18
	v_mov_b32_e32 v18, v157
	v_lshlrev_b32_e32 v157, 16, v83
	v_pk_mul_f32 v[110:111], v[188:189], v[188:189]
	v_lshlrev_b32_e32 v119, 16, v141
	v_and_b32_e32 v121, 0xffff0000, v141
	v_lshlrev_b32_e32 v125, 16, v140
	v_and_b32_e32 v127, 0xffff0000, v140
	v_mov_b32_e32 v140, v102
	v_mov_b32_e32 v141, v6
	v_mov_b32_e32 v6, v103
	v_pk_mul_f32 v[102:103], v[156:157], v[156:157]
	v_and_b32_e32 v185, 0xffff0000, v83
	v_add_f32_e32 v70, v111, v71
	v_mov_b32_e32 v134, v104
	v_mov_b32_e32 v135, v8
	v_mov_b32_e32 v8, v105
	v_lshlrev_b32_e32 v153, 16, v84
	v_pk_mul_f32 v[104:105], v[184:185], v[184:185]
	v_add_f32_e32 v70, v103, v70
	v_pk_mul_f32 v[180:181], v[152:153], v[152:153]
	v_and_b32_e32 v155, 0xffff0000, v84
	v_add_f32_e32 v70, v105, v70
	v_lshlrev_b32_e32 v130, 16, v143
	v_and_b32_e32 v132, 0xffff0000, v143
	v_lshlrev_b32_e32 v143, 16, v85
	v_pk_mul_f32 v[182:183], v[154:155], v[154:155]
	v_add_f32_e32 v70, v181, v70
	v_lshlrev_b32_e32 v118, 16, v145
	v_and_b32_e32 v120, 0xffff0000, v145
	v_pk_mul_f32 v[176:177], v[142:143], v[142:143]
	v_and_b32_e32 v145, 0xffff0000, v85
	v_add_f32_e32 v70, v183, v70
	v_pk_mul_f32 v[178:179], v[144:145], v[144:145]
	v_add_f32_e32 v70, v177, v70
	v_pk_mul_f32 v[172:173], v[136:137], v[136:137]
	v_add_f32_e32 v70, v179, v70
	v_pk_mul_f32 v[174:175], v[138:139], v[138:139]
	v_add_f32_e32 v70, v173, v70
	v_add_f32_e32 v70, v175, v70
	v_fmac_f32_e32 v70, v131, v131
	v_fmac_f32_e32 v70, v133, v133
	v_fmac_f32_e32 v70, v125, v125
	v_fmac_f32_e32 v70, v127, v127
	v_fmac_f32_e32 v70, v119, v119
	v_fmac_f32_e32 v70, v121, v121
	v_add_f32_e32 v103, v72, v70
	v_add_f32_e32 v103, v110, v103
	v_add_f32_e32 v102, v102, v103
	v_add_f32_e32 v173, v104, v102
	v_add_f32_e32 v173, v180, v173
	v_add_f32_e32 v173, v182, v173
	v_add_f32_e32 v173, v176, v173
	v_add_f32_e32 v173, v178, v173
	v_mov_b32_e32 v176, v132
	v_mov_b32_e32 v177, v130
	s_waitcnt vmcnt(16)
	v_mov_b32_e32 v179, v24
	v_add_f32_e32 v24, v172, v173
	v_lshlrev_b64 v[10:11], 8, v[30:31]
	v_pk_mul_f32 v[176:177], v[176:177], v[176:177]
	v_add_f32_e32 v24, v174, v24
	v_lshl_add_u64 v[10:11], s[10:11], 0, v[10:11]
	v_lshlrev_b32_e32 v12, 6, v169
	v_mov_b32_e32 v13, v149
	v_mov_b32_e32 v180, v126
	v_mov_b32_e32 v181, v124
	v_add_f32_e32 v24, v177, v24
	v_lshl_add_u64 v[170:171], v[10:11], 0, v[12:13]
	v_pk_mul_f32 v[180:181], v[180:181], v[180:181]
	v_add_f32_e32 v24, v176, v24
	global_load_dwordx4 v[10:13], v[170:171], off offset:48
	global_load_dwordx4 v[14:17], v[170:171], off offset:32
	global_load_dwordx4 v[30:33], v[170:171], off offset:16
	global_load_dwordx4 v[34:37], v[170:171], off
	v_mov_b32_e32 v122, v112
	v_mov_b32_e32 v123, v4
	v_mov_b32_e32 v4, v113
	global_load_dwordx4 v[70:73], v[170:171], off offset:176
	global_load_dwordx4 v[82:85], v[170:171], off offset:160
	global_load_dwordx4 v[102:105], v[170:171], off offset:144
	global_load_dwordx4 v[110:113], v[170:171], off offset:128
	v_mov_b32_e32 v170, v120
	v_mov_b32_e32 v171, v118
	v_add_f32_e32 v24, v181, v24
	v_pk_mul_f32 v[170:171], v[170:171], v[170:171]
	v_add_f32_e32 v24, v180, v24
	v_add_f32_e32 v24, v171, v24
	v_add_f32_e32 v24, v170, v24
	v_mov_b32_e32 v178, v28
	v_mov_b32_e32 v28, v24
	s_nop 1
	v_permlane32_swap_b32_e32 v24, v28
	v_add_f32_e32 v24, v24, v28
	v_fmamk_f32 v24, v24, 0x3baaaaab, v163
	v_mul_f32_e32 v28, 0x4b800000, v24
	v_cmp_gt_f32_e32 vcc, s69, v24
	s_nop 1
	v_cndmask_b32_e32 v24, v24, v28, vcc
	v_rsq_f32_e32 v170, v24
	v_mov_b32_e32 v24, v29
	v_mov_b32_e32 v29, v22
	v_mov_b32_e32 v28, v26
	v_mul_f32_e32 v22, 0x45800000, v170
	v_cndmask_b32_e32 v22, v170, v22, vcc
	v_mul_f32_e32 v26, 0x3dd53b94, v22
	s_waitcnt vmcnt(22)
	v_mul_f32_e32 v22, v114, v26
	v_mul_f32_e32 v114, v22, v190
	v_mul_f32_e32 v22, v106, v26
	v_mul_f32_e32 v106, v22, v194
	v_mul_f32_e32 v22, v115, v26
	v_mul_f32_e32 v115, v22, v191
	v_mul_f32_e32 v22, v107, v26
	v_mul_f32_e32 v107, v22, v195
	v_mul_f32_e32 v22, v116, v26
	v_mul_f32_e32 v116, v22, v192
	v_mul_f32_e32 v22, v108, v26
	v_mul_f32_e32 v108, v22, v196
	v_mul_f32_e32 v22, v117, v26
	v_mul_f32_e32 v117, v22, v193
	v_mul_f32_e32 v22, v109, v26
	v_mul_f32_e32 v109, v22, v197
	s_waitcnt vmcnt(20)
	v_mul_f32_e32 v22, v98, v26
	v_mul_f32_e32 v170, v22, v198
	v_mul_f32_e32 v22, v94, v26
	v_mul_f32_e32 v94, v22, v202
	v_mul_f32_e32 v22, v99, v26
	v_mul_f32_e32 v171, v22, v199
	v_mul_f32_e32 v22, v95, v26
	v_mul_f32_e32 v95, v22, v203
	v_mul_f32_e32 v22, v100, v26
	v_mul_f32_e32 v172, v22, v200
	v_mul_f32_e32 v22, v96, v26
	v_mul_f32_e32 v96, v22, v204
	v_mul_f32_e32 v22, v101, v26
	v_mul_f32_e32 v173, v22, v201
	v_mul_f32_e32 v22, v97, v26
	v_mul_f32_e32 v97, v22, v205
	s_waitcnt vmcnt(18)
	v_mul_f32_e32 v22, v90, v26
	v_mul_f32_e32 v90, v22, v206
	v_mul_f32_e32 v22, v86, v26
	v_mul_f32_e32 v86, v22, v210
	v_mul_f32_e32 v22, v91, v26
	v_mul_f32_e32 v91, v22, v207
	v_mul_f32_e32 v22, v87, v26
	v_mul_f32_e32 v87, v22, v211
	v_mul_f32_e32 v22, v92, v26
	v_mul_f32_e32 v92, v22, v208
	v_mul_f32_e32 v22, v88, v26
	v_mul_f32_e32 v88, v22, v212
	v_mul_f32_e32 v22, v93, v26
	v_mul_f32_e32 v93, v22, v209
	v_mul_f32_e32 v22, v89, v26
	v_mul_f32_e32 v89, v22, v213
	s_waitcnt vmcnt(16)
	v_mul_f32_e32 v22, v78, v26
	v_mul_f32_e32 v78, v22, v214
	v_mul_f32_e32 v22, v74, v26
	v_mul_f32_e32 v74, v22, v218
	v_mul_f32_e32 v22, v79, v26
	v_mul_f32_e32 v79, v22, v215
	v_mul_f32_e32 v22, v75, v26
	v_mul_f32_e32 v75, v22, v219
	v_mul_f32_e32 v22, v80, v26
	v_mul_f32_e32 v80, v22, v216
	v_mul_f32_e32 v22, v76, v26
	v_mul_f32_e32 v76, v22, v220
	v_mul_f32_e32 v22, v81, v26
	v_mul_f32_e32 v81, v22, v217
	v_mul_f32_e32 v22, v77, v26
	v_mul_f32_e32 v77, v22, v221
	s_waitcnt vmcnt(14)
	v_mul_f32_e32 v22, v66, v26
	v_mul_f32_e32 v66, v22, v222
	v_mul_f32_e32 v22, v26, v62
	v_mul_f32_e32 v62, v22, v226
	v_mul_f32_e32 v22, v67, v26
	v_mul_f32_e32 v67, v22, v223
	v_mul_f32_e32 v22, v26, v63
	v_mul_f32_e32 v63, v22, v227
	v_mul_f32_e32 v22, v68, v26
	v_mul_f32_e32 v68, v22, v224
	v_mul_f32_e32 v22, v26, v64
	v_mul_f32_e32 v64, v22, v228
	v_mul_f32_e32 v22, v69, v26
	v_mul_f32_e32 v69, v22, v225
	v_mul_f32_e32 v22, v26, v65
	v_mul_f32_e32 v65, v22, v229
	s_waitcnt vmcnt(12)
	v_mul_f32_e32 v22, v26, v58
	v_mul_f32_e32 v58, v22, v230
	v_mul_f32_e32 v22, v26, v54
	v_mul_f32_e32 v54, v22, v234
	v_mul_f32_e32 v22, v26, v59
	v_mul_f32_e32 v59, v22, v231
	v_mul_f32_e32 v22, v26, v55
	v_mul_f32_e32 v55, v22, v235
	v_mul_f32_e32 v22, v26, v60
	v_mul_f32_e32 v60, v22, v232
	v_mul_f32_e32 v22, v26, v56
	v_mul_f32_e32 v56, v22, v236
	v_mul_f32_e32 v22, v26, v61
	v_mul_f32_e32 v61, v22, v233
	v_mul_f32_e32 v22, v26, v57
	v_mul_f32_e32 v57, v22, v237
	s_waitcnt vmcnt(10)
	v_mul_f32_e32 v22, v26, v50
	v_mul_f32_e32 v174, v22, v238
	v_mul_f32_e32 v22, v26, v46
	v_mul_f32_e32 v175, v22, v242
	v_mul_f32_e32 v22, v26, v51
	v_mul_f32_e32 v176, v22, v239
	v_mul_f32_e32 v22, v26, v47
	v_mul_f32_e32 v177, v22, v243
	v_mul_f32_e32 v22, v26, v52
	v_mul_f32_e32 v52, v22, v240
	v_mul_f32_e32 v22, v26, v48
	v_mul_f32_e32 v180, v22, v244
	v_mul_f32_e32 v22, v26, v53
	v_mul_f32_e32 v53, v22, v241
	v_mul_f32_e32 v22, v26, v49
	v_mul_f32_e32 v181, v22, v245
	s_waitcnt vmcnt(8)
	v_mul_f32_e32 v22, v26, v42
	v_mul_f32_e32 v182, v22, v246
	v_mul_f32_e32 v22, v26, v38
	v_mul_f32_e32 v183, v22, v250
	v_mul_f32_e32 v22, v26, v43
	v_mul_f32_e32 v190, v22, v247
	v_mul_f32_e32 v22, v26, v39
	v_mul_f32_e32 v191, v22, v251
	v_mul_f32_e32 v22, v26, v44
	v_mul_f32_e32 v192, v22, v248
	v_mul_f32_e32 v22, v26, v40
	v_mul_f32_e32 v193, v22, v252
	v_mul_f32_e32 v22, v26, v45
	v_mul_f32_e32 v194, v22, v249
	v_mul_f32_e32 v22, v26, v41
	v_pk_mul_f32 v[28:29], v[26:27], v[28:29] op_sel_hi:[0,1]
	v_mul_f32_e32 v195, v22, v253
	v_pk_mul_f32 v[28:29], v[28:29], v[186:187]
	v_mov_b32_e32 v22, v27
	v_pk_mul_f32 v[38:39], v[26:27], v[158:159] op_sel_hi:[0,1]
	v_pk_mul_f32 v[22:23], v[26:27], v[22:23] op_sel_hi:[0,1]
	v_pk_mul_f32 v[18:19], v[26:27], v[18:19] op_sel_hi:[0,1]
	v_pk_mul_f32 v[40:41], v[26:27], v[178:179] op_sel_hi:[0,1]
	v_pk_mul_f32 v[42:43], v[26:27], v[150:151] op_sel_hi:[0,1]
	v_pk_mul_f32 v[24:25], v[26:27], v[24:25] op_sel_hi:[0,1]
	v_pk_mul_f32 v[20:21], v[26:27], v[20:21] op_sel_hi:[0,1]
	v_pk_mul_f32 v[44:45], v[26:27], v[140:141] op_sel_hi:[0,1]
	v_pk_mul_f32 v[46:47], v[26:27], v[128:129] op_sel_hi:[0,1]
	v_pk_mul_f32 v[6:7], v[26:27], v[6:7] op_sel_hi:[0,1]
	v_pk_mul_f32 v[2:3], v[26:27], v[2:3] op_sel_hi:[0,1]
	v_pk_mul_f32 v[48:49], v[26:27], v[134:135] op_sel_hi:[0,1]
	v_pk_mul_f32 v[50:51], v[26:27], v[122:123] op_sel_hi:[0,1]
	v_pk_mul_f32 v[8:9], v[26:27], v[8:9] op_sel_hi:[0,1]
	v_pk_mul_f32 v[4:5], v[26:27], v[4:5] op_sel_hi:[0,1]
	s_waitcnt vmcnt(4)
	v_pk_mul_f32 v[26:27], v[28:29], v[34:35] op_sel:[1,0] op_sel_hi:[0,1]
	v_pk_mul_f32 v[22:23], v[22:23], v[188:189]
	v_pk_mul_f32 v[48:49], v[48:49], v[130:131]
	v_sub_f32_e32 v130, v26, v27
	v_pk_mul_f32 v[26:27], v[28:29], v[34:35]
	v_pk_mul_f32 v[40:41], v[40:41], v[156:157]
	v_add_f32_e32 v28, v27, v26
	v_pk_mul_f32 v[26:27], v[22:23], v[36:37] op_sel:[1,0] op_sel_hi:[0,1]
	v_pk_mul_f32 v[22:23], v[22:23], v[36:37]
	v_sub_f32_e32 v26, v26, v27
	v_add_f32_e32 v27, v23, v22
	v_pk_mul_f32 v[22:23], v[40:41], v[30:31] op_sel:[1,0] op_sel_hi:[0,1]
	v_pk_mul_f32 v[24:25], v[24:25], v[184:185]
	v_sub_f32_e32 v29, v22, v23
	v_pk_mul_f32 v[22:23], v[40:41], v[30:31]
	v_pk_mul_f32 v[38:39], v[38:39], v[152:153]
	v_add_f32_e32 v30, v23, v22
	v_pk_mul_f32 v[22:23], v[24:25], v[32:33] op_sel:[1,0] op_sel_hi:[0,1]
	v_sub_f32_e32 v31, v22, v23
	v_pk_mul_f32 v[22:23], v[24:25], v[32:33]
	v_pk_mul_f32 v[18:19], v[18:19], v[154:155]
	v_add_f32_e32 v24, v23, v22
	v_pk_mul_f32 v[22:23], v[38:39], v[14:15] op_sel:[1,0] op_sel_hi:[0,1]
	v_pk_mul_f32 v[14:15], v[38:39], v[14:15]
	v_sub_f32_e32 v22, v22, v23
	v_add_f32_e32 v23, v15, v14
	v_pk_mul_f32 v[14:15], v[18:19], v[16:17] op_sel:[1,0] op_sel_hi:[0,1]
	v_pk_mul_f32 v[42:43], v[42:43], v[142:143]
	v_sub_f32_e32 v25, v14, v15
	v_pk_mul_f32 v[14:15], v[18:19], v[16:17]
	v_pk_mul_f32 v[20:21], v[20:21], v[144:145]
	v_add_f32_e32 v16, v15, v14
	v_pk_mul_f32 v[14:15], v[42:43], v[10:11] op_sel:[1,0] op_sel_hi:[0,1]
	v_pk_mul_f32 v[10:11], v[42:43], v[10:11]
	v_sub_f32_e32 v14, v14, v15
	v_add_f32_e32 v15, v11, v10
	v_pk_mul_f32 v[10:11], v[20:21], v[12:13] op_sel:[1,0] op_sel_hi:[0,1]
	v_pk_mul_f32 v[44:45], v[44:45], v[136:137]
	v_sub_f32_e32 v17, v10, v11
	v_pk_mul_f32 v[10:11], v[20:21], v[12:13]
	v_pk_mul_f32 v[6:7], v[6:7], v[138:139]
	v_add_f32_e32 v12, v11, v10
	s_waitcnt vmcnt(0)
	v_pk_mul_f32 v[10:11], v[44:45], v[110:111] op_sel:[1,0] op_sel_hi:[0,1]
	v_sub_f32_e32 v13, v10, v11
	v_pk_mul_f32 v[10:11], v[44:45], v[110:111]
	v_pk_mul_f32 v[8:9], v[8:9], v[132:133]
	v_add_f32_e32 v18, v11, v10
	v_pk_mul_f32 v[10:11], v[6:7], v[112:113] op_sel:[1,0] op_sel_hi:[0,1]
	v_pk_mul_f32 v[6:7], v[6:7], v[112:113]
	v_sub_f32_e32 v10, v10, v11
	v_add_f32_e32 v11, v7, v6
	v_pk_mul_f32 v[6:7], v[48:49], v[102:103] op_sel:[1,0] op_sel_hi:[0,1]
	v_sub_f32_e32 v19, v6, v7
	v_pk_mul_f32 v[6:7], v[48:49], v[102:103]
	v_pk_mul_f32 v[46:47], v[46:47], v[124:125]
	v_add_f32_e32 v20, v7, v6
	v_pk_mul_f32 v[6:7], v[8:9], v[104:105] op_sel:[1,0] op_sel_hi:[0,1]
	v_sub_f32_e32 v21, v6, v7
	v_pk_mul_f32 v[6:7], v[8:9], v[104:105]
	v_pk_mul_f32 v[2:3], v[2:3], v[126:127]
	v_add_f32_e32 v8, v7, v6
	v_pk_mul_f32 v[6:7], v[46:47], v[82:83] op_sel:[1,0] op_sel_hi:[0,1]
	v_sub_f32_e32 v9, v6, v7
	v_pk_mul_f32 v[6:7], v[46:47], v[82:83]
	v_pk_mul_f32 v[50:51], v[50:51], v[118:119]
	v_add_f32_e32 v32, v7, v6
	v_pk_mul_f32 v[6:7], v[2:3], v[84:85] op_sel:[1,0] op_sel_hi:[0,1]
	v_pk_mul_f32 v[2:3], v[2:3], v[84:85]
	v_sub_f32_e32 v6, v6, v7
	v_add_f32_e32 v7, v3, v2
	v_pk_mul_f32 v[2:3], v[50:51], v[70:71] op_sel:[1,0] op_sel_hi:[0,1]
	v_pk_mul_f32 v[4:5], v[4:5], v[120:121]
	v_sub_f32_e32 v33, v2, v3
	v_pk_mul_f32 v[2:3], v[50:51], v[70:71]
	v_cvt_pk_bf16_f32 v98, v114, v115
	v_cvt_pk_bf16_f32 v99, v116, v117
	v_cvt_pk_bf16_f32 v100, v106, v107
	v_cvt_pk_bf16_f32 v101, v108, v109
	v_cvt_pk_bf16_f32 v102, v170, v171
	s_nop 0
	v_add_f32_e32 v34, v3, v2
	v_pk_mul_f32 v[2:3], v[4:5], v[72:73] op_sel:[1,0] op_sel_hi:[0,1]
	v_sub_f32_e32 v35, v2, v3
	v_pk_mul_f32 v[2:3], v[4:5], v[72:73]
	v_cvt_pk_bf16_f32 v103, v172, v173
	v_cvt_pk_bf16_f32 v104, v94, v95
	v_cvt_pk_bf16_f32 v105, v96, v97
	v_cvt_pk_bf16_f32 v106, v90, v91
	v_cvt_pk_bf16_f32 v107, v92, v93
	s_nop 0
	v_add_f32_e32 v2, v3, v2
	v_cvt_pk_bf16_f32 v108, v86, v87
	v_cvt_pk_bf16_f32 v109, v88, v89
	v_cvt_pk_bf16_f32 v110, v78, v79
	v_cvt_pk_bf16_f32 v111, v80, v81
	v_cvt_pk_bf16_f32 v112, v74, v75
	v_cvt_pk_bf16_f32 v113, v76, v77
	v_cvt_pk_bf16_f32 v114, v66, v67
	v_cvt_pk_bf16_f32 v115, v68, v69
	v_cvt_pk_bf16_f32 v116, v62, v63
	v_cvt_pk_bf16_f32 v117, v64, v65
	v_cvt_pk_bf16_f32 v118, v58, v59
	v_cvt_pk_bf16_f32 v119, v60, v61
	v_cvt_pk_bf16_f32 v120, v54, v55
	v_cvt_pk_bf16_f32 v121, v56, v57
	v_cvt_pk_bf16_f32 v122, v174, v176
	v_cvt_pk_bf16_f32 v123, v52, v53
	v_cvt_pk_bf16_f32 v124, v175, v177
	v_cvt_pk_bf16_f32 v125, v180, v181
	v_cvt_pk_bf16_f32 v126, v182, v190
	v_cvt_pk_bf16_f32 v127, v192, v194
	v_cvt_pk_bf16_f32 v128, v183, v191
	v_cvt_pk_bf16_f32 v129, v193, v195
	v_cvt_pk_bf16_f32 v130, v130, v26
	v_cvt_pk_bf16_f32 v131, v29, v31
	v_cvt_pk_bf16_f32 v132, v22, v25
	v_cvt_pk_bf16_f32 v133, v14, v17
	v_cvt_pk_bf16_f32 v134, v13, v10
	v_cvt_pk_bf16_f32 v135, v19, v21
	v_cvt_pk_bf16_f32 v136, v9, v6
	v_cvt_pk_bf16_f32 v137, v33, v35
	v_cvt_pk_bf16_f32 v138, v28, v27
	v_cvt_pk_bf16_f32 v139, v30, v24
	v_cvt_pk_bf16_f32 v140, v23, v16
	v_cvt_pk_bf16_f32 v141, v15, v12
	v_cvt_pk_bf16_f32 v142, v18, v11
	v_cvt_pk_bf16_f32 v143, v20, v8
	v_cvt_pk_bf16_f32 v144, v32, v7
	v_cvt_pk_bf16_f32 v145, v34, v2
	v_mul_hi_i32 v2, v168, s70
	v_lshrrev_b32_e32 v3, 31, v2
	v_ashrrev_i32_e32 v2, 2, v2
	v_add_u32_e32 v2, v2, v3
	v_mul_lo_u32 v3, v2, 24
	v_sub_u32_e32 v3, v168, v3
	v_lshrrev_b32_e32 v16, 1, v2
	v_bitop3_b32 v3, v16, v3, 7 bitop3:0x6c
	v_mul_lo_u32 v2, v2, s68
	v_lshl_add_u32 v2, v3, 4, v2
	v_add_u32_e32 v3, 0x200, v168
	v_mul_hi_i32 v4, v3, s70
	v_lshrrev_b32_e32 v5, 31, v4
	v_ashrrev_i32_e32 v4, 2, v4
	v_add_u32_e32 v4, v4, v5
	v_mul_lo_u32 v5, v4, 24
	v_sub_u32_e32 v5, v3, v5
	v_lshrrev_b32_e32 v16, 1, v4
	v_bitop3_b32 v5, v16, v5, 7 bitop3:0x6c
	v_mul_lo_u32 v4, v4, s68
	v_lshl_add_u32 v4, v5, 4, v4
	v_add_u32_e32 v5, 0x400, v168
	v_mul_hi_i32 v6, v5, s70
	v_lshrrev_b32_e32 v7, 31, v6
	v_ashrrev_i32_e32 v6, 2, v6
	v_add_u32_e32 v6, v6, v7
	v_mul_lo_u32 v7, v6, 24
	v_sub_u32_e32 v5, v5, v7
	v_lshrrev_b32_e32 v16, 1, v6
	v_bitop3_b32 v5, v16, v5, 7 bitop3:0x6c
	v_mul_lo_u32 v6, v6, s68
	v_ashrrev_i32_e32 v9, 4, v168
	v_lshl_add_u32 v6, v5, 4, v6
	v_bfe_u32 v5, v168, 2, 2
	v_lshrrev_b32_e32 v7, 1, v168
	v_and_b32_e32 v10, 0x1ffff0, v9
	v_lshrrev_b32_e32 v9, 1, v9
	v_ashrrev_i32_e32 v3, 4, v3
	v_and_or_b32 v5, v7, 8, v5
	v_and_b32_e32 v7, 0x60, v168
	v_lshlrev_b32_e32 v8, 3, v168
	v_and_b32_e32 v9, 4, v9
	v_and_b32_e32 v11, 0x1ffff0, v3
	v_lshrrev_b32_e32 v3, 1, v3
	v_and_or_b32 v7, v8, 24, v7
	v_or3_b32 v9, v10, v9, v5
	v_and_b32_e32 v3, 4, v3
	s_barrier
	global_load_lds_dwordx4 v2, s[44:45]
	s_mov_b32 m0, s72
	v_lshlrev_b32_e32 v7, 1, v7
	v_lshlrev_b32_e32 v10, 11, v9
	v_or3_b32 v3, v11, v3, v5
	global_load_lds_dwordx4 v4, s[44:45]
	s_mov_b32 m0, s73
	v_or_b32_e32 v9, v10, v7
	v_lshlrev_b32_e32 v11, 11, v3
	global_load_lds_dwordx4 v6, s[44:45]
	s_mov_b32 m0, s64
	v_or_b32_e32 v3, v11, v7
	global_load_lds_dwordx4 v9, s[46:47]
	s_mov_b32 m0, s74
	v_lshlrev_b32_e32 v13, 1, v168
	global_load_lds_dwordx4 v3, s[46:47]
	v_lshlrev_b32_e32 v9, 4, v168
	v_and_b32_e32 v14, 32, v13
	v_or_b32_e32 v3, 32, v148
	v_and_b32_e32 v16, 0x13, v167
	v_and_b32_e32 v17, 4, v167
	v_lshl_or_b32 v16, v17, 1, v16
	v_and_b32_e32 v17, 8, v167
	v_lshrrev_b32_e32 v17, 1, v17
	v_or_b32_e32 v16, v16, v17
	v_mul_u32_u24_e32 v5, 0x180, v16
	v_lshlrev_b32_e32 v17, 3, v16
	v_and_b32_e32 v7, 0x70, v17
	v_and_b32_e32 v12, 0xc0, v9
	v_and_or_b32 v8, v8, s75, v14
	v_bitop3_b32 v172, v3, v5, v7 bitop3:0xde
	v_or_b32_e32 v3, 64, v148
	v_mul_i32_i24_e32 v15, -8, v169
	v_add3_u32 v169, v12, 0, v8
	v_and_b32_e32 v12, 0xc0, v13
	v_and_b32_e32 v13, 48, v9
	v_bitop3_b32 v173, v3, v5, v7 bitop3:0xde
	v_or_b32_e32 v3, 0x60, v148
	v_or3_b32 v8, v11, v12, v13
	v_mov_b32_e32 v9, v149
	v_bitop3_b32 v171, v148, v5, v7 bitop3:0xde
	v_bitop3_b32 v174, v3, v5, v7 bitop3:0xde
	v_mov_b32_e32 v3, v149
	v_mov_b32_e32 v5, v149
	v_mov_b32_e32 v7, v149
	v_lshl_add_u64 v[150:151], s[48:49], 0, v[8:9]
	v_mov_b32_e32 v240, v8
	v_or3_b32 v8, v10, v12, v13
	v_mov_b32_e32 v16, v149
	v_mov_b32_e32 v17, v149
	v_and_b32_e32 v170, 63, v168
	s_lshl_b32 s46, s80, 2
	v_lshl_add_u32 v168, v167, 2, s65
	v_lshl_add_u64 v[152:153], s[48:49], 0, v[8:9]
	v_mov_b32_e32 v241, v8
	v_lshl_add_u64 v[154:155], s[50:51], 0, v[6:7]
	v_mov_b32_e32 v242, v6
	v_lshl_add_u64 v[156:157], s[50:51], 0, v[4:5]
	v_mov_b32_e32 v243, v4
	v_lshl_add_u64 v[158:159], s[50:51], 0, v[2:3]
	v_mov_b32_e32 v244, v2
	s_add_u32 s94, s2, s50
	s_addc_u32 s95, s3, s51
	s_add_u32 s96, s2, s48
	s_addc_u32 s97, s3, s49
	v_add3_u32 v167, s63, v15, v167
	v_mov_b32_e32 v2, v149
	v_mov_b32_e32 v4, v149
	v_mov_b32_e32 v6, v149
	v_mov_b32_e32 v8, v149
	v_mov_b32_e32 v10, v149
	v_mov_b32_e32 v11, v149
	v_mov_b32_e32 v12, v149
	v_mov_b32_e32 v13, v149
	v_mov_b32_e32 v14, v149
	v_mov_b32_e32 v15, v149
	v_mov_b64_e32 v[32:33], v[16:17]
	v_mov_b64_e32 v[48:49], v[16:17]
	v_mov_b64_e32 v[64:65], v[16:17]
	s_add_i32 s46, s46, 4
	v_cmp_gt_u32_e64 s[0:1], 32, v170
	v_mov_b32_e32 v176, 0
	v_mov_b32_e32 v175, 0
	v_mov_b32_e32 v210, 0
	v_mov_b32_e32 v211, 0
	v_mov_b32_e32 v212, 0
	v_mov_b32_e32 v213, 0
	v_mov_b32_e32 v214, 0
	v_mov_b32_e32 v215, 0
	v_mov_b32_e32 v216, 0
	v_mov_b32_e32 v217, 0
	v_mov_b32_e32 v218, 0
	v_mov_b32_e32 v219, 0
	v_mov_b32_e32 v220, 0
	v_mov_b32_e32 v221, 0
	v_mov_b32_e32 v222, 0
	v_mov_b32_e32 v223, 0
	v_mov_b32_e32 v224, 0
	v_mov_b32_e32 v225, 0
	s_movk_i32 s47, 0xff00
	v_mov_b64_e32 v[30:31], v[14:15]
	v_mov_b64_e32 v[28:29], v[12:13]
	v_mov_b64_e32 v[26:27], v[10:11]
	v_mov_b64_e32 v[24:25], v[8:9]
	v_mov_b64_e32 v[22:23], v[6:7]
	v_mov_b64_e32 v[20:21], v[4:5]
	v_mov_b64_e32 v[18:19], v[2:3]
	v_mov_b64_e32 v[46:47], v[14:15]
	v_mov_b64_e32 v[44:45], v[12:13]
	v_mov_b64_e32 v[42:43], v[10:11]
	v_mov_b64_e32 v[40:41], v[8:9]
	v_mov_b64_e32 v[38:39], v[6:7]
	v_mov_b64_e32 v[36:37], v[4:5]
	v_mov_b64_e32 v[34:35], v[2:3]
	v_mov_b64_e32 v[62:63], v[14:15]
	v_mov_b64_e32 v[60:61], v[12:13]
	v_mov_b64_e32 v[58:59], v[10:11]
	v_mov_b64_e32 v[56:57], v[8:9]
	v_mov_b64_e32 v[54:55], v[6:7]
	v_mov_b64_e32 v[52:53], v[4:5]
	v_mov_b64_e32 v[50:51], v[2:3]

.LBB0_958:
	s_or_b64 exec, exec, s[44:45]
	s_waitcnt lgkmcnt(0)
	s_lshl_b64 s[0:1], s[52:53], 11
	s_add_u32 s0, s61, s0
	s_addc_u32 s1, s62, s1
	s_add_u32 s0, s0, s79
	s_addc_u32 s1, s1, 0
	s_mov_b32 s44, 0x05040100
	v_and_b32_e32 v85, 3, v164
	v_lshl_add_u32 v83, v85, 8, v85
	v_add_u32_e32 v83, 0x0c0c0400, v83
	v_lshrrev_b32_e32 v87, 5, v164
	v_lshl_add_u32 v84, v87, 2, v85
	v_lshlrev_b32_e32 v84, 11, v84
	v_and_b32_e32 v85, 28, v164
	v_add_u32_e32 v84, v84, v85
	v_lshl_add_u32 v87, v87, 4, s65
	ds_read_b128 v[66:69], v87 offset:128
	v_mov_b32_e32 v86, v84
	s_waitcnt lgkmcnt(0)
	v_mul_f32_e32 v66, 0x41800000, v66
	v_mul_f32_e32 v67, 0x41800000, v67
	v_mul_f32_e32 v68, 0x41800000, v68
	v_mul_f32_e32 v69, 0x41800000, v69
	v_mul_f32_e32 v70, v50, v66
	v_mul_f32_e32 v71, v51, v67
	v_mul_f32_e32 v72, v52, v68
	v_mul_f32_e32 v73, v53, v69
	v_med3_f32 v70, v70, s77, v166
	v_med3_f32 v71, v71, s77, v166
	v_med3_f32 v72, v72, s77, v166
	v_med3_f32 v73, v73, s77, v166
	v_cvt_pk_fp8_f32 v74, v70, v71
	v_cvt_pk_fp8_f32 v74, v72, v73 op_sel:[0,0,1]
	s_nop 1
	v_mov_b32_dpp v75, v74 quad_perm:[0,0,0,0] row_mask:0xf bank_mask:0xf
	v_mov_b32_dpp v76, v74 quad_perm:[1,1,1,1] row_mask:0xf bank_mask:0xf
	v_mov_b32_dpp v77, v74 quad_perm:[2,2,2,2] row_mask:0xf bank_mask:0xf
	v_mov_b32_dpp v78, v74 quad_perm:[3,3,3,3] row_mask:0xf bank_mask:0xf
	v_perm_b32 v80, v76, v75, v83
	v_perm_b32 v81, v78, v77, v83
	v_perm_b32 v82, v81, v80, s44
	global_store_dword v86, v82, s[0:1]
	v_mul_f32_e32 v70, v34, v66
	v_mul_f32_e32 v71, v35, v67
	v_mul_f32_e32 v72, v36, v68
	v_mul_f32_e32 v73, v37, v69
	v_med3_f32 v70, v70, s77, v166
	v_med3_f32 v71, v71, s77, v166
	v_med3_f32 v72, v72, s77, v166
	v_med3_f32 v73, v73, s77, v166
	v_cvt_pk_fp8_f32 v74, v70, v71
	v_cvt_pk_fp8_f32 v74, v72, v73 op_sel:[0,0,1]
	s_nop 1
	v_mov_b32_dpp v75, v74 quad_perm:[0,0,0,0] row_mask:0xf bank_mask:0xf
	v_mov_b32_dpp v76, v74 quad_perm:[1,1,1,1] row_mask:0xf bank_mask:0xf
	v_mov_b32_dpp v77, v74 quad_perm:[2,2,2,2] row_mask:0xf bank_mask:0xf
	v_mov_b32_dpp v78, v74 quad_perm:[3,3,3,3] row_mask:0xf bank_mask:0xf
	v_perm_b32 v80, v76, v75, v83
	v_perm_b32 v81, v78, v77, v83
	v_perm_b32 v82, v81, v80, s44
	global_store_dword v86, v82, s[0:1] offset:32
	v_mul_f32_e32 v70, v18, v66
	v_mul_f32_e32 v71, v19, v67
	v_mul_f32_e32 v72, v20, v68
	v_mul_f32_e32 v73, v21, v69
	v_med3_f32 v70, v70, s77, v166
	v_med3_f32 v71, v71, s77, v166
	v_med3_f32 v72, v72, s77, v166
	v_med3_f32 v73, v73, s77, v166
	v_cvt_pk_fp8_f32 v74, v70, v71
	v_cvt_pk_fp8_f32 v74, v72, v73 op_sel:[0,0,1]
	s_nop 1
	v_mov_b32_dpp v75, v74 quad_perm:[0,0,0,0] row_mask:0xf bank_mask:0xf
	v_mov_b32_dpp v76, v74 quad_perm:[1,1,1,1] row_mask:0xf bank_mask:0xf
	v_mov_b32_dpp v77, v74 quad_perm:[2,2,2,2] row_mask:0xf bank_mask:0xf
	v_mov_b32_dpp v78, v74 quad_perm:[3,3,3,3] row_mask:0xf bank_mask:0xf
	v_perm_b32 v80, v76, v75, v83
	v_perm_b32 v81, v78, v77, v83
	v_perm_b32 v82, v81, v80, s44
	global_store_dword v86, v82, s[0:1] offset:64
	v_mul_f32_e32 v70, v2, v66
	v_mul_f32_e32 v71, v3, v67
	v_mul_f32_e32 v72, v4, v68
	v_mul_f32_e32 v73, v5, v69
	v_med3_f32 v70, v70, s77, v166
	v_med3_f32 v71, v71, s77, v166
	v_med3_f32 v72, v72, s77, v166
	v_med3_f32 v73, v73, s77, v166
	v_cvt_pk_fp8_f32 v74, v70, v71
	v_cvt_pk_fp8_f32 v74, v72, v73 op_sel:[0,0,1]
	s_nop 1
	v_mov_b32_dpp v75, v74 quad_perm:[0,0,0,0] row_mask:0xf bank_mask:0xf
	v_mov_b32_dpp v76, v74 quad_perm:[1,1,1,1] row_mask:0xf bank_mask:0xf
	v_mov_b32_dpp v77, v74 quad_perm:[2,2,2,2] row_mask:0xf bank_mask:0xf
	v_mov_b32_dpp v78, v74 quad_perm:[3,3,3,3] row_mask:0xf bank_mask:0xf
	v_perm_b32 v80, v76, v75, v83
	v_perm_b32 v81, v78, v77, v83
	v_perm_b32 v82, v81, v80, s44
	global_store_dword v86, v82, s[0:1] offset:96
	ds_read_b128 v[66:69], v87 offset:160
	v_add_u32_e32 v86, 0x4000, v84
	s_waitcnt lgkmcnt(0)
	v_mul_f32_e32 v66, 0x41800000, v66
	v_mul_f32_e32 v67, 0x41800000, v67
	v_mul_f32_e32 v68, 0x41800000, v68
	v_mul_f32_e32 v69, 0x41800000, v69
	v_mul_f32_e32 v70, v54, v66
	v_mul_f32_e32 v71, v55, v67
	v_mul_f32_e32 v72, v56, v68
	v_mul_f32_e32 v73, v57, v69
	v_med3_f32 v70, v70, s77, v166
	v_med3_f32 v71, v71, s77, v166
	v_med3_f32 v72, v72, s77, v166
	v_med3_f32 v73, v73, s77, v166
	v_cvt_pk_fp8_f32 v74, v70, v71
	v_cvt_pk_fp8_f32 v74, v72, v73 op_sel:[0,0,1]
	s_nop 1
	v_mov_b32_dpp v75, v74 quad_perm:[0,0,0,0] row_mask:0xf bank_mask:0xf
	v_mov_b32_dpp v76, v74 quad_perm:[1,1,1,1] row_mask:0xf bank_mask:0xf
	v_mov_b32_dpp v77, v74 quad_perm:[2,2,2,2] row_mask:0xf bank_mask:0xf
	v_mov_b32_dpp v78, v74 quad_perm:[3,3,3,3] row_mask:0xf bank_mask:0xf
	v_perm_b32 v80, v76, v75, v83
	v_perm_b32 v81, v78, v77, v83
	v_perm_b32 v82, v81, v80, s44
	global_store_dword v86, v82, s[0:1]
	v_mul_f32_e32 v70, v38, v66
	v_mul_f32_e32 v71, v39, v67
	v_mul_f32_e32 v72, v40, v68
	v_mul_f32_e32 v73, v41, v69
	v_med3_f32 v70, v70, s77, v166
	v_med3_f32 v71, v71, s77, v166
	v_med3_f32 v72, v72, s77, v166
	v_med3_f32 v73, v73, s77, v166
	v_cvt_pk_fp8_f32 v74, v70, v71
	v_cvt_pk_fp8_f32 v74, v72, v73 op_sel:[0,0,1]
	s_nop 1
	v_mov_b32_dpp v75, v74 quad_perm:[0,0,0,0] row_mask:0xf bank_mask:0xf
	v_mov_b32_dpp v76, v74 quad_perm:[1,1,1,1] row_mask:0xf bank_mask:0xf
	v_mov_b32_dpp v77, v74 quad_perm:[2,2,2,2] row_mask:0xf bank_mask:0xf
	v_mov_b32_dpp v78, v74 quad_perm:[3,3,3,3] row_mask:0xf bank_mask:0xf
	v_perm_b32 v80, v76, v75, v83
	v_perm_b32 v81, v78, v77, v83
	v_perm_b32 v82, v81, v80, s44
	global_store_dword v86, v82, s[0:1] offset:32
	v_mul_f32_e32 v70, v22, v66
	v_mul_f32_e32 v71, v23, v67
	v_mul_f32_e32 v72, v24, v68
	v_mul_f32_e32 v73, v25, v69
	v_med3_f32 v70, v70, s77, v166
	v_med3_f32 v71, v71, s77, v166
	v_med3_f32 v72, v72, s77, v166
	v_med3_f32 v73, v73, s77, v166
	v_cvt_pk_fp8_f32 v74, v70, v71
	v_cvt_pk_fp8_f32 v74, v72, v73 op_sel:[0,0,1]
	s_nop 1
	v_mov_b32_dpp v75, v74 quad_perm:[0,0,0,0] row_mask:0xf bank_mask:0xf
	v_mov_b32_dpp v76, v74 quad_perm:[1,1,1,1] row_mask:0xf bank_mask:0xf
	v_mov_b32_dpp v77, v74 quad_perm:[2,2,2,2] row_mask:0xf bank_mask:0xf
	v_mov_b32_dpp v78, v74 quad_perm:[3,3,3,3] row_mask:0xf bank_mask:0xf
	v_perm_b32 v80, v76, v75, v83
	v_perm_b32 v81, v78, v77, v83
	v_perm_b32 v82, v81, v80, s44
	global_store_dword v86, v82, s[0:1] offset:64
	v_mul_f32_e32 v70, v6, v66
	v_mul_f32_e32 v71, v7, v67
	v_mul_f32_e32 v72, v8, v68
	v_mul_f32_e32 v73, v9, v69
	v_med3_f32 v70, v70, s77, v166
	v_med3_f32 v71, v71, s77, v166
	v_med3_f32 v72, v72, s77, v166
	v_med3_f32 v73, v73, s77, v166
	v_cvt_pk_fp8_f32 v74, v70, v71
	v_cvt_pk_fp8_f32 v74, v72, v73 op_sel:[0,0,1]
	s_nop 1
	v_mov_b32_dpp v75, v74 quad_perm:[0,0,0,0] row_mask:0xf bank_mask:0xf
	v_mov_b32_dpp v76, v74 quad_perm:[1,1,1,1] row_mask:0xf bank_mask:0xf
	v_mov_b32_dpp v77, v74 quad_perm:[2,2,2,2] row_mask:0xf bank_mask:0xf
	v_mov_b32_dpp v78, v74 quad_perm:[3,3,3,3] row_mask:0xf bank_mask:0xf
	v_perm_b32 v80, v76, v75, v83
	v_perm_b32 v81, v78, v77, v83
	v_perm_b32 v82, v81, v80, s44
	global_store_dword v86, v82, s[0:1] offset:96
	ds_read_b128 v[66:69], v87 offset:192
	v_add_u32_e32 v86, 0x8000, v84
	s_waitcnt lgkmcnt(0)
	v_mul_f32_e32 v66, 0x41800000, v66
	v_mul_f32_e32 v67, 0x41800000, v67
	v_mul_f32_e32 v68, 0x41800000, v68
	v_mul_f32_e32 v69, 0x41800000, v69
	v_mul_f32_e32 v70, v58, v66
	v_mul_f32_e32 v71, v59, v67
	v_mul_f32_e32 v72, v60, v68
	v_mul_f32_e32 v73, v61, v69
	v_med3_f32 v70, v70, s77, v166
	v_med3_f32 v71, v71, s77, v166
	v_med3_f32 v72, v72, s77, v166
	v_med3_f32 v73, v73, s77, v166
	v_cvt_pk_fp8_f32 v74, v70, v71
	v_cvt_pk_fp8_f32 v74, v72, v73 op_sel:[0,0,1]
	s_nop 1
	v_mov_b32_dpp v75, v74 quad_perm:[0,0,0,0] row_mask:0xf bank_mask:0xf
	v_mov_b32_dpp v76, v74 quad_perm:[1,1,1,1] row_mask:0xf bank_mask:0xf
	v_mov_b32_dpp v77, v74 quad_perm:[2,2,2,2] row_mask:0xf bank_mask:0xf
	v_mov_b32_dpp v78, v74 quad_perm:[3,3,3,3] row_mask:0xf bank_mask:0xf
	v_perm_b32 v80, v76, v75, v83
	v_perm_b32 v81, v78, v77, v83
	v_perm_b32 v82, v81, v80, s44
	global_store_dword v86, v82, s[0:1]
	v_mul_f32_e32 v70, v42, v66
	v_mul_f32_e32 v71, v43, v67
	v_mul_f32_e32 v72, v44, v68
	v_mul_f32_e32 v73, v45, v69
	v_med3_f32 v70, v70, s77, v166
	v_med3_f32 v71, v71, s77, v166
	v_med3_f32 v72, v72, s77, v166
	v_med3_f32 v73, v73, s77, v166
	v_cvt_pk_fp8_f32 v74, v70, v71
	v_cvt_pk_fp8_f32 v74, v72, v73 op_sel:[0,0,1]
	s_nop 1
	v_mov_b32_dpp v75, v74 quad_perm:[0,0,0,0] row_mask:0xf bank_mask:0xf
	v_mov_b32_dpp v76, v74 quad_perm:[1,1,1,1] row_mask:0xf bank_mask:0xf
	v_mov_b32_dpp v77, v74 quad_perm:[2,2,2,2] row_mask:0xf bank_mask:0xf
	v_mov_b32_dpp v78, v74 quad_perm:[3,3,3,3] row_mask:0xf bank_mask:0xf
	v_perm_b32 v80, v76, v75, v83
	v_perm_b32 v81, v78, v77, v83
	v_perm_b32 v82, v81, v80, s44
	global_store_dword v86, v82, s[0:1] offset:32
	v_mul_f32_e32 v70, v26, v66
	v_mul_f32_e32 v71, v27, v67
	v_mul_f32_e32 v72, v28, v68
	v_mul_f32_e32 v73, v29, v69
	v_med3_f32 v70, v70, s77, v166
	v_med3_f32 v71, v71, s77, v166
	v_med3_f32 v72, v72, s77, v166
	v_med3_f32 v73, v73, s77, v166
	v_cvt_pk_fp8_f32 v74, v70, v71
	v_cvt_pk_fp8_f32 v74, v72, v73 op_sel:[0,0,1]
	s_nop 1
	v_mov_b32_dpp v75, v74 quad_perm:[0,0,0,0] row_mask:0xf bank_mask:0xf
	v_mov_b32_dpp v76, v74 quad_perm:[1,1,1,1] row_mask:0xf bank_mask:0xf
	v_mov_b32_dpp v77, v74 quad_perm:[2,2,2,2] row_mask:0xf bank_mask:0xf
	v_mov_b32_dpp v78, v74 quad_perm:[3,3,3,3] row_mask:0xf bank_mask:0xf
	v_perm_b32 v80, v76, v75, v83
	v_perm_b32 v81, v78, v77, v83
	v_perm_b32 v82, v81, v80, s44
	global_store_dword v86, v82, s[0:1] offset:64
	v_mul_f32_e32 v70, v10, v66
	v_mul_f32_e32 v71, v11, v67
	v_mul_f32_e32 v72, v12, v68
	v_mul_f32_e32 v73, v13, v69
	v_med3_f32 v70, v70, s77, v166
	v_med3_f32 v71, v71, s77, v166
	v_med3_f32 v72, v72, s77, v166
	v_med3_f32 v73, v73, s77, v166
	v_cvt_pk_fp8_f32 v74, v70, v71
	v_cvt_pk_fp8_f32 v74, v72, v73 op_sel:[0,0,1]
	s_nop 1
	v_mov_b32_dpp v75, v74 quad_perm:[0,0,0,0] row_mask:0xf bank_mask:0xf
	v_mov_b32_dpp v76, v74 quad_perm:[1,1,1,1] row_mask:0xf bank_mask:0xf
	v_mov_b32_dpp v77, v74 quad_perm:[2,2,2,2] row_mask:0xf bank_mask:0xf
	v_mov_b32_dpp v78, v74 quad_perm:[3,3,3,3] row_mask:0xf bank_mask:0xf
	v_perm_b32 v80, v76, v75, v83
	v_perm_b32 v81, v78, v77, v83
	v_perm_b32 v82, v81, v80, s44
	global_store_dword v86, v82, s[0:1] offset:96
	ds_read_b128 v[66:69], v87 offset:224
	v_add_u32_e32 v86, 0xc000, v84
	s_waitcnt lgkmcnt(0)
	v_mul_f32_e32 v66, 0x41800000, v66
	v_mul_f32_e32 v67, 0x41800000, v67
	v_mul_f32_e32 v68, 0x41800000, v68
	v_mul_f32_e32 v69, 0x41800000, v69
	v_mul_f32_e32 v70, v62, v66
	v_mul_f32_e32 v71, v63, v67
	v_mul_f32_e32 v72, v64, v68
	v_mul_f32_e32 v73, v65, v69
	v_med3_f32 v70, v70, s77, v166
	v_med3_f32 v71, v71, s77, v166
	v_med3_f32 v72, v72, s77, v166
	v_med3_f32 v73, v73, s77, v166
	v_cvt_pk_fp8_f32 v74, v70, v71
	v_cvt_pk_fp8_f32 v74, v72, v73 op_sel:[0,0,1]
	s_nop 1
	v_mov_b32_dpp v75, v74 quad_perm:[0,0,0,0] row_mask:0xf bank_mask:0xf
	v_mov_b32_dpp v76, v74 quad_perm:[1,1,1,1] row_mask:0xf bank_mask:0xf
	v_mov_b32_dpp v77, v74 quad_perm:[2,2,2,2] row_mask:0xf bank_mask:0xf
	v_mov_b32_dpp v78, v74 quad_perm:[3,3,3,3] row_mask:0xf bank_mask:0xf
	v_perm_b32 v80, v76, v75, v83
	v_perm_b32 v81, v78, v77, v83
	v_perm_b32 v82, v81, v80, s44
	global_store_dword v86, v82, s[0:1]
	v_mul_f32_e32 v70, v46, v66
	v_mul_f32_e32 v71, v47, v67
	v_mul_f32_e32 v72, v48, v68
	v_mul_f32_e32 v73, v49, v69
	v_med3_f32 v70, v70, s77, v166
	v_med3_f32 v71, v71, s77, v166
	v_med3_f32 v72, v72, s77, v166
	v_med3_f32 v73, v73, s77, v166
	v_cvt_pk_fp8_f32 v74, v70, v71
	v_cvt_pk_fp8_f32 v74, v72, v73 op_sel:[0,0,1]
	s_nop 1
	v_mov_b32_dpp v75, v74 quad_perm:[0,0,0,0] row_mask:0xf bank_mask:0xf
	v_mov_b32_dpp v76, v74 quad_perm:[1,1,1,1] row_mask:0xf bank_mask:0xf
	v_mov_b32_dpp v77, v74 quad_perm:[2,2,2,2] row_mask:0xf bank_mask:0xf
	v_mov_b32_dpp v78, v74 quad_perm:[3,3,3,3] row_mask:0xf bank_mask:0xf
	v_perm_b32 v80, v76, v75, v83
	v_perm_b32 v81, v78, v77, v83
	v_perm_b32 v82, v81, v80, s44
	global_store_dword v86, v82, s[0:1] offset:32
	v_mul_f32_e32 v70, v30, v66
	v_mul_f32_e32 v71, v31, v67
	v_mul_f32_e32 v72, v32, v68
	v_mul_f32_e32 v73, v33, v69
	v_med3_f32 v70, v70, s77, v166
	v_med3_f32 v71, v71, s77, v166
	v_med3_f32 v72, v72, s77, v166
	v_med3_f32 v73, v73, s77, v166
	v_cvt_pk_fp8_f32 v74, v70, v71
	v_cvt_pk_fp8_f32 v74, v72, v73 op_sel:[0,0,1]
	s_nop 1
	v_mov_b32_dpp v75, v74 quad_perm:[0,0,0,0] row_mask:0xf bank_mask:0xf
	v_mov_b32_dpp v76, v74 quad_perm:[1,1,1,1] row_mask:0xf bank_mask:0xf
	v_mov_b32_dpp v77, v74 quad_perm:[2,2,2,2] row_mask:0xf bank_mask:0xf
	v_mov_b32_dpp v78, v74 quad_perm:[3,3,3,3] row_mask:0xf bank_mask:0xf
	v_perm_b32 v80, v76, v75, v83
	v_perm_b32 v81, v78, v77, v83
	v_perm_b32 v82, v81, v80, s44
	global_store_dword v86, v82, s[0:1] offset:64
	v_mul_f32_e32 v70, v14, v66
	v_mul_f32_e32 v71, v15, v67
	v_mul_f32_e32 v72, v16, v68
	v_mul_f32_e32 v73, v17, v69
	v_med3_f32 v70, v70, s77, v166
	v_med3_f32 v71, v71, s77, v166
	v_med3_f32 v72, v72, s77, v166
	v_med3_f32 v73, v73, s77, v166
	v_cvt_pk_fp8_f32 v74, v70, v71
	v_cvt_pk_fp8_f32 v74, v72, v73 op_sel:[0,0,1]
	s_nop 1
	v_mov_b32_dpp v75, v74 quad_perm:[0,0,0,0] row_mask:0xf bank_mask:0xf
	v_mov_b32_dpp v76, v74 quad_perm:[1,1,1,1] row_mask:0xf bank_mask:0xf
	v_mov_b32_dpp v77, v74 quad_perm:[2,2,2,2] row_mask:0xf bank_mask:0xf
	v_mov_b32_dpp v78, v74 quad_perm:[3,3,3,3] row_mask:0xf bank_mask:0xf
	v_perm_b32 v80, v76, v75, v83
	v_perm_b32 v81, v78, v77, v83
	v_perm_b32 v82, v81, v80, s44
	global_store_dword v86, v82, s[0:1] offset:96
	s_branch .LBB0_803


